# M4: M2 + kernarg pointer loads hoisted to kernel entry in K1 (3 lazy s_loads in the epilogue) and K3 (mid-prologue s_load that stalled PART load issue)
# speedup vs baseline: 1.0301x; 1.0301x over previous
_Z12gemm1_kernelPKfS0_S0_PDv8_DF16_PDF16_S3_:
	s_and_b32 s3, s2, 7
	s_ashr_i32 s2, s2, 3
	s_mul_hi_i32 s8, s2, 0x2aaaaaab
	s_lshr_b32 s9, s8, 31
	s_ashr_i32 s8, s8, 1
	s_mul_i32 s3, s3, 3
	s_add_i32 s8, s8, s9
	s_load_dwordx4 s[4:7], s[0:1], 0x0
	s_load_dwordx2 s[10:11], s[0:1], 0x10
	s_load_dwordx2 s[12:13], s[0:1], 0x18
	s_load_dwordx2 s[14:15], s[0:1], 0x20
	s_load_dwordx2 s[16:17], s[0:1], 0x28
	s_add_i32 s3, s3, s8
	s_mul_i32 s8, s8, 12
	v_bfe_u32 v85, v0, 6, 2
	s_sub_i32 s8, s2, s8
	v_lshlrev_b32_e32 v1, 5, v85
	s_ashr_i32 s9, s8, 31
	v_lshl_or_b32 v1, s3, 7, v1
	s_lshl_b64 s[2:3], s[8:9], 17
	v_bfe_u32 v18, v0, 3, 3
	v_lshlrev_b32_e32 v4, 5, v0
	v_and_b32_e32 v6, 0x100, v0
	v_or_b32_e32 v2, v1, v18
	s_waitcnt lgkmcnt(0)
	s_add_u32 s2, s6, s2
	v_and_b32_e32 v4, 0x1800, v4
	v_and_b32_e32 v84, 63, v0
	v_mov_b32_e32 v67, 0
	v_ashrrev_i32_e32 v3, 31, v2
	s_addc_u32 s3, s7, s3
	v_lshl_or_b32 v66, v6, 8, v4
	v_lshlrev_b64 v[2:3], 11, v[2:3]
	v_lshl_add_u64 v[4:5], s[2:3], 0, v[66:67]
	v_lshlrev_b32_e32 v66, 2, v84
	v_and_b32_e32 v78, 7, v0
	v_lshl_add_u64 v[68:69], v[4:5], 0, v[66:67]
	v_lshl_add_u64 v[2:3], s[4:5], 0, v[2:3]
	v_lshlrev_b32_e32 v4, 2, v6
	v_mov_b32_e32 v5, v67
	v_lshl_add_u64 v[2:3], v[2:3], 0, v[4:5]
	v_lshlrev_b32_e32 v4, 4, v78
	v_lshl_add_u64 v[70:71], v[2:3], 0, v[4:5]
	s_movk_i32 s4, 0x4000
	v_add_co_u32_e32 v72, vcc, s4, v70
	global_load_dwordx4 v[2:5], v[70:71], off
	s_nop 0
	v_addc_co_u32_e32 v73, vcc, 0, v71, vcc
	global_load_dwordx4 v[6:9], v[72:73], off
	s_mov_b32 s3, 0x8000
	global_load_dword v20, v[68:69], off
	global_load_dword v21, v[68:69], off offset:1792
	global_load_dword v22, v[68:69], off offset:1536
	global_load_dword v23, v[68:69], off offset:1280
	global_load_dword v24, v[68:69], off offset:1024
	global_load_dword v25, v[68:69], off offset:768
	global_load_dword v26, v[68:69], off offset:512
	global_load_dword v27, v[68:69], off offset:256
	v_add_co_u32_e32 v76, vcc, s3, v70
	v_and_b32_e32 v79, 31, v0
	s_nop 0
	v_addc_co_u32_e32 v77, vcc, 0, v71, vcc
	global_load_dwordx4 v[10:13], v[76:77], off
	s_mov_b32 s2, 0xc000
	v_lshrrev_b32_e32 v19, 6, v0
	v_mul_u32_u24_e32 v29, 0x50, v18
	v_lshl_or_b32 v18, s8, 7, v79
	v_add_co_u32_e32 v74, vcc, s2, v70
	v_mul_u32_u24_e32 v28, 0x1400, v19
	v_ashrrev_i32_e32 v19, 31, v18
	v_addc_co_u32_e32 v75, vcc, 0, v71, vcc
	v_lshl_add_u64 v[18:19], v[18:19], 2, s[10:11]
	global_load_dwordx4 v[14:17], v[74:75], off
	global_load_dword v80, v[18:19], off
	global_load_dword v83, v[18:19], off offset:128
	global_load_dword v81, v[18:19], off offset:256
	global_load_dword v82, v[18:19], off offset:384
	v_lshrrev_b32_e32 v86, 8, v0
	v_mov_b32_e32 v18, 0xa000
	s_movk_i32 s5, 0x2000
	v_lshl_add_u32 v32, v86, 13, v18
	v_add_co_u32_e32 v18, vcc, s5, v68
	global_load_dwordx4 v[62:65], v[70:71], off offset:128
	global_load_dwordx4 v[58:61], v[72:73], off offset:128
	global_load_dwordx4 v[54:57], v[76:77], off offset:128
	global_load_dwordx4 v[50:53], v[74:75], off offset:128
	v_addc_co_u32_e32 v19, vcc, 0, v69, vcc
	global_load_dword v91, v[18:19], off offset:1792
	global_load_dword v104, v[18:19], off offset:1536
	global_load_dword v105, v[18:19], off offset:1280
	global_load_dword v106, v[18:19], off offset:1024
	global_load_dword v107, v[18:19], off offset:768
	global_load_dword v108, v[18:19], off offset:512
	global_load_dword v109, v[18:19], off offset:256
	global_load_dword v110, v[18:19], off
	v_bfe_u32 v67, v0, 5, 1
	v_mul_u32_u24_e32 v30, 0x50, v79
	v_lshlrev_b32_e32 v31, 4, v67
	v_add3_u32 v89, v28, v30, v31
	v_lshl_or_b32 v88, v84, 4, v32
	s_waitcnt vmcnt(18)
	v_mov_b32_e32 v33, v3
	v_mov_b32_e32 v3, v5
	v_lshlrev_b32_e32 v5, 4, v0
	v_mov_b32_e32 v19, v8
	v_cvt_pk_f16_f32 v8, v20, v27
	v_and_b32_e32 v5, 0x800, v5
	v_lshlrev_b32_e32 v20, 10, v67
	v_or3_b32 v5, v32, v5, v20
	v_lshlrev_b32_e32 v20, 3, v0
	v_mov_b32_e32 v18, v9
	s_waitcnt vmcnt(17)
	v_mov_b32_e32 v35, v11
	v_cvt_pk_f16_f32 v11, v22, v21
	v_and_b32_e32 v20, 0x200, v20
	v_lshlrev_b32_e32 v21, 4, v79
	v_or3_b32 v87, v5, v20, v21
	v_or_b32_e32 v5, v28, v29
	v_mov_b32_e32 v34, v10
	v_cvt_pk_f16_f32 v10, v24, v23
	v_cvt_pk_f16_f32 v9, v26, v25
	v_lshl_add_u32 v90, v78, 3, v5
	v_cvt_pk_f16_f32 v3, v4, v3
	v_cvt_pk_f16_f32 v2, v2, v33
	v_cvt_pk_f16_f32 v5, v19, v18
	v_cvt_pk_f16_f32 v4, v6, v7
	s_waitcnt vmcnt(16)
	ds_write_b128 v87, v[8:11]
	ds_write2_b64 v90, v[2:3], v[4:5] offset1:80
	v_cvt_pk_f16_f32 v3, v12, v13
	v_cvt_pk_f16_f32 v2, v34, v35
	v_cvt_pk_f16_f32 v5, v16, v17
	v_cvt_pk_f16_f32 v4, v14, v15
	ds_write2_b64 v90, v[2:3], v[4:5] offset0:160 offset1:240
	v_add_co_u32_e32 v2, vcc, s4, v68
	global_load_dwordx4 v[34:37], v[70:71], off offset:256
	global_load_dwordx4 v[38:41], v[72:73], off offset:256
	global_load_dwordx4 v[42:45], v[76:77], off offset:256
	global_load_dwordx4 v[46:49], v[74:75], off offset:256
	v_addc_co_u32_e32 v3, vcc, 0, v69, vcc
	global_load_dword v111, v[2:3], off offset:1792
	global_load_dword v112, v[2:3], off offset:1536
	global_load_dword v113, v[2:3], off offset:1280
	global_load_dword v114, v[2:3], off offset:1024
	global_load_dword v115, v[2:3], off offset:768
	global_load_dword v116, v[2:3], off offset:512
	global_load_dword v117, v[2:3], off offset:256
	global_load_dword v118, v[2:3], off
	s_waitcnt lgkmcnt(0)
	s_barrier
	ds_read_b128 v[2:5], v89
	ds_read_b128 v[6:9], v88
	ds_read_b128 v[92:95], v89 offset:32
	ds_read_b128 v[10:13], v88 offset:1024
	s_waitcnt lgkmcnt(2)
	v_mfma_f32_32x32x16_f16 v[18:33], v[2:5], v[6:9], 0
	ds_read_b128 v[96:99], v88 offset:2048
	ds_read_b128 v[100:103], v88 offset:3072
	s_waitcnt vmcnt(12)
	s_movk_i32 s4, 0x6000
	s_waitcnt lgkmcnt(2)
	v_mfma_f32_32x32x16_f16 v[2:17], v[2:5], v[10:13], 0
	s_waitcnt lgkmcnt(1)
	v_mfma_f32_32x32x16_f16 v[18:33], v[92:95], v[96:99], v[18:33]
	v_mov_b32_e32 v96, v53
	v_mov_b32_e32 v97, v56
	v_mov_b32_e32 v98, v52
	v_mov_b32_e32 v99, v57
	s_waitcnt lgkmcnt(0)
	v_mfma_f32_32x32x16_f16 v[2:17], v[92:95], v[100:103], v[2:17]
	v_mov_b32_e32 v92, v60
	v_mov_b32_e32 v93, v63
	v_mov_b32_e32 v94, v62
	v_mov_b32_e32 v95, v61
	v_cvt_pk_f16_f32 v63, v104, v91
	v_cvt_pk_f16_f32 v62, v106, v105
	v_cvt_pk_f16_f32 v61, v108, v107
	v_cvt_pk_f16_f32 v60, v110, v109
	v_cvt_pk_f16_f32 v53, v64, v65
	v_cvt_pk_f16_f32 v52, v94, v93
	v_cvt_pk_f16_f32 v57, v92, v95
	v_cvt_pk_f16_f32 v56, v58, v59
	v_add_u32_e32 v91, 0x800, v90
	ds_write_b128 v87, v[60:63] offset:4096
	ds_write2_b64 v91, v[52:53], v[56:57] offset0:64 offset1:144
	v_cvt_pk_f16_f32 v53, v97, v99
	v_cvt_pk_f16_f32 v52, v54, v55
	v_cvt_pk_f16_f32 v55, v98, v96
	v_cvt_pk_f16_f32 v54, v50, v51
	v_add_u32_e32 v92, 0xc00, v90
	v_add_co_u32_e32 v94, vcc, s4, v68
	ds_write2_b64 v92, v[52:53], v[54:55] offset0:96 offset1:176
	s_nop 0
	v_addc_co_u32_e32 v95, vcc, 0, v69, vcc
	global_load_dwordx4 v[50:53], v[70:71], off offset:384
	global_load_dwordx4 v[54:57], v[72:73], off offset:384
	global_load_dwordx4 v[58:61], v[76:77], off offset:384
	global_load_dwordx4 v[62:65], v[74:75], off offset:384
	global_load_dword v93, v[94:95], off offset:1792
	global_load_dword v110, v[94:95], off offset:1536
	global_load_dword v119, v[94:95], off offset:1280
	global_load_dword v120, v[94:95], off offset:1024
	global_load_dword v121, v[94:95], off offset:768
	global_load_dword v122, v[94:95], off offset:512
	global_load_dword v123, v[94:95], off offset:256
	global_load_dword v124, v[94:95], off
	s_waitcnt lgkmcnt(0)
	s_barrier
	ds_read_b128 v[94:97], v89 offset:2560
	ds_read_b128 v[98:101], v88 offset:4096
	ds_read_b128 v[102:105], v89 offset:2592
	ds_read_b128 v[106:109], v88 offset:5120
	s_waitcnt lgkmcnt(2)
	v_mfma_f32_32x32x16_f16 v[18:33], v[94:97], v[98:101], v[18:33]
	s_waitcnt lgkmcnt(0)
	v_mfma_f32_32x32x16_f16 v[2:17], v[94:97], v[106:109], v[2:17]
	ds_read_b128 v[94:97], v88 offset:6144
	ds_read_b128 v[98:101], v88 offset:7168
	s_waitcnt vmcnt(12)
	s_waitcnt lgkmcnt(1)
	v_mfma_f32_32x32x16_f16 v[18:33], v[102:105], v[94:97], v[18:33]
	v_mov_b32_e32 v94, v37
	v_mov_b32_e32 v95, v39
	v_mov_b32_e32 v96, v36
	v_mov_b32_e32 v97, v38
	v_cvt_pk_f16_f32 v39, v112, v111
	v_cvt_pk_f16_f32 v38, v114, v113
	v_cvt_pk_f16_f32 v37, v116, v115
	v_cvt_pk_f16_f32 v36, v118, v117
	ds_write_b128 v87, v[36:39]
	v_cvt_pk_f16_f32 v37, v96, v94
	v_cvt_pk_f16_f32 v36, v34, v35
	v_cvt_pk_f16_f32 v35, v40, v41
	v_cvt_pk_f16_f32 v34, v97, v95
	ds_write2_b64 v90, v[36:37], v[34:35] offset1:80
	v_cvt_pk_f16_f32 v35, v44, v45
	v_cvt_pk_f16_f32 v34, v42, v43
	v_cvt_pk_f16_f32 v37, v48, v49
	v_cvt_pk_f16_f32 v36, v46, v47
	v_add_co_u32_e32 v94, vcc, s3, v68
	s_waitcnt lgkmcnt(2)
	v_mfma_f32_32x32x16_f16 v[2:17], v[102:105], v[98:101], v[2:17]
	ds_write2_b64 v90, v[34:35], v[36:37] offset0:160 offset1:240
	v_addc_co_u32_e32 v95, vcc, 0, v69, vcc
	global_load_dwordx4 v[34:37], v[70:71], off offset:512
	global_load_dwordx4 v[38:41], v[72:73], off offset:512
	global_load_dwordx4 v[42:45], v[76:77], off offset:512
	global_load_dwordx4 v[46:49], v[74:75], off offset:512
	global_load_dword v111, v[94:95], off offset:1792
	global_load_dword v112, v[94:95], off offset:1536
	global_load_dword v113, v[94:95], off offset:1280
	global_load_dword v114, v[94:95], off offset:1024
	global_load_dword v115, v[94:95], off offset:768
	global_load_dword v116, v[94:95], off offset:512
	global_load_dword v117, v[94:95], off offset:256
	global_load_dword v118, v[94:95], off
	s_waitcnt lgkmcnt(0)
	s_barrier
	ds_read_b128 v[94:97], v89
	ds_read_b128 v[98:101], v88
	ds_read_b128 v[102:105], v89 offset:32
	ds_read_b128 v[106:109], v88 offset:1024
	s_waitcnt lgkmcnt(2)
	v_mfma_f32_32x32x16_f16 v[18:33], v[94:97], v[98:101], v[18:33]
	s_mov_b32 s3, 0xa000
	s_waitcnt lgkmcnt(0)
	v_mfma_f32_32x32x16_f16 v[2:17], v[94:97], v[106:109], v[2:17]
	ds_read_b128 v[94:97], v88 offset:2048
	ds_read_b128 v[98:101], v88 offset:3072
	s_waitcnt vmcnt(12)
	s_waitcnt lgkmcnt(1)
	v_mfma_f32_32x32x16_f16 v[18:33], v[102:105], v[94:97], v[18:33]
	v_mov_b32_e32 v94, v51
	v_mov_b32_e32 v95, v61
	v_mov_b32_e32 v96, v63
	v_mov_b32_e32 v97, v60
	v_cvt_pk_f16_f32 v63, v110, v93
	v_cvt_pk_f16_f32 v61, v122, v121
	s_waitcnt lgkmcnt(0)
	v_mfma_f32_32x32x16_f16 v[2:17], v[102:105], v[98:101], v[2:17]
	v_mov_b32_e32 v98, v62
	v_cvt_pk_f16_f32 v62, v120, v119
	v_cvt_pk_f16_f32 v60, v124, v123
	v_cvt_pk_f16_f32 v51, v52, v53
	v_cvt_pk_f16_f32 v50, v50, v94
	v_cvt_pk_f16_f32 v53, v56, v57
	v_cvt_pk_f16_f32 v52, v54, v55
	ds_write_b128 v87, v[60:63] offset:4096
	ds_write2_b64 v91, v[50:51], v[52:53] offset0:64 offset1:144
	v_cvt_pk_f16_f32 v51, v97, v95
	v_cvt_pk_f16_f32 v50, v58, v59
	v_cvt_pk_f16_f32 v53, v64, v65
	v_cvt_pk_f16_f32 v52, v98, v96
	v_add_co_u32_e32 v94, vcc, s3, v68
	ds_write2_b64 v92, v[50:51], v[52:53] offset0:96 offset1:176
	s_nop 0
	v_addc_co_u32_e32 v95, vcc, 0, v69, vcc
	global_load_dwordx4 v[50:53], v[70:71], off offset:640
	global_load_dwordx4 v[54:57], v[72:73], off offset:640
	global_load_dwordx4 v[58:61], v[76:77], off offset:640
	global_load_dwordx4 v[62:65], v[74:75], off offset:640
	global_load_dword v93, v[94:95], off offset:1792
	global_load_dword v110, v[94:95], off offset:1536
	global_load_dword v119, v[94:95], off offset:1280
	global_load_dword v120, v[94:95], off offset:1024
	global_load_dword v121, v[94:95], off offset:768
	global_load_dword v122, v[94:95], off offset:512
	global_load_dword v123, v[94:95], off offset:256
	global_load_dword v124, v[94:95], off
	s_waitcnt lgkmcnt(0)
	s_barrier
	ds_read_b128 v[94:97], v89 offset:2560
	ds_read_b128 v[98:101], v88 offset:4096
	ds_read_b128 v[102:105], v89 offset:2592
	ds_read_b128 v[106:109], v88 offset:5120
	s_waitcnt lgkmcnt(2)
	v_mfma_f32_32x32x16_f16 v[18:33], v[94:97], v[98:101], v[18:33]
	s_waitcnt lgkmcnt(0)
	v_mfma_f32_32x32x16_f16 v[2:17], v[94:97], v[106:109], v[2:17]
	ds_read_b128 v[94:97], v88 offset:6144
	ds_read_b128 v[98:101], v88 offset:7168
	s_waitcnt vmcnt(12)
	s_waitcnt lgkmcnt(1)
	v_mfma_f32_32x32x16_f16 v[18:33], v[102:105], v[94:97], v[18:33]
	v_mov_b32_e32 v94, v41
	v_mov_b32_e32 v95, v40
	v_mov_b32_e32 v96, v35
	v_mov_b32_e32 v35, v37
	v_mov_b32_e32 v97, v42
	v_cvt_pk_f16_f32 v42, v114, v113
	s_waitcnt lgkmcnt(0)
	v_mfma_f32_32x32x16_f16 v[2:17], v[102:105], v[98:101], v[2:17]
	v_mov_b32_e32 v98, v43
	v_cvt_pk_f16_f32 v43, v112, v111
	v_cvt_pk_f16_f32 v41, v116, v115
	v_cvt_pk_f16_f32 v40, v118, v117
	v_cvt_pk_f16_f32 v35, v36, v35
	v_cvt_pk_f16_f32 v34, v34, v96
	v_cvt_pk_f16_f32 v37, v95, v94
	v_cvt_pk_f16_f32 v36, v38, v39
	ds_write_b128 v87, v[40:43]
	ds_write2_b64 v90, v[34:35], v[36:37] offset1:80
	v_cvt_pk_f16_f32 v35, v44, v45
	v_cvt_pk_f16_f32 v34, v97, v98
	v_cvt_pk_f16_f32 v37, v48, v49
	v_cvt_pk_f16_f32 v36, v46, v47
	v_add_co_u32_e32 v94, vcc, s2, v68
	ds_write2_b64 v90, v[34:35], v[36:37] offset0:160 offset1:240
	s_nop 0
	v_addc_co_u32_e32 v95, vcc, 0, v69, vcc
	global_load_dwordx4 v[34:37], v[70:71], off offset:768
	global_load_dwordx4 v[38:41], v[72:73], off offset:768
	global_load_dwordx4 v[42:45], v[76:77], off offset:768
	global_load_dwordx4 v[46:49], v[74:75], off offset:768
	global_load_dword v111, v[94:95], off offset:1792
	global_load_dword v112, v[94:95], off offset:1536
	global_load_dword v113, v[94:95], off offset:1280
	global_load_dword v114, v[94:95], off offset:1024
	global_load_dword v115, v[94:95], off offset:768
	global_load_dword v116, v[94:95], off offset:512
	global_load_dword v117, v[94:95], off offset:256
	global_load_dword v118, v[94:95], off
	s_waitcnt lgkmcnt(0)
	s_barrier
	ds_read_b128 v[94:97], v89
	ds_read_b128 v[98:101], v88
	ds_read_b128 v[102:105], v89 offset:32
	ds_read_b128 v[106:109], v88 offset:1024
	s_waitcnt lgkmcnt(0)
	v_mfma_f32_32x32x16_f16 v[2:17], v[94:97], v[106:109], v[2:17]
	s_mov_b32 s2, 0xe000
	v_add_co_u32_e32 v68, vcc, s2, v68
	v_cmp_eq_u32_e64 s[2:3], 1, v86
	s_nop 0
	v_addc_co_u32_e32 v69, vcc, 0, v69, vcc
	v_cmp_ne_u32_e32 vcc, 1, v86
	v_mfma_f32_32x32x16_f16 v[18:33], v[94:97], v[98:101], v[18:33]
	ds_read_b128 v[94:97], v88 offset:2048
	ds_read_b128 v[98:101], v88 offset:3072
	s_waitcnt vmcnt(12)
	s_waitcnt lgkmcnt(0)
	v_mfma_f32_32x32x16_f16 v[2:17], v[102:105], v[98:101], v[2:17]
	v_mov_b32_e32 v98, v51
	v_mov_b32_e32 v51, v53
	v_mov_b32_e32 v53, v57
	v_mov_b32_e32 v57, v65
	v_cvt_pk_f16_f32 v51, v52, v51
	v_cvt_pk_f16_f32 v50, v50, v98
	v_mfma_f32_32x32x16_f16 v[18:33], v[102:105], v[94:97], v[18:33]
	v_cvt_pk_f16_f32 v97, v110, v93
	v_cvt_pk_f16_f32 v96, v120, v119
	v_cvt_pk_f16_f32 v95, v122, v121
	v_cvt_pk_f16_f32 v94, v124, v123
	v_cvt_pk_f16_f32 v53, v56, v53
	v_cvt_pk_f16_f32 v52, v54, v55
	ds_write_b128 v87, v[94:97] offset:4096
	ds_write2_b64 v91, v[50:51], v[52:53] offset0:64 offset1:144
	v_cvt_pk_f16_f32 v51, v60, v61
	v_cvt_pk_f16_f32 v50, v58, v59
	v_cvt_pk_f16_f32 v53, v64, v57
	v_cvt_pk_f16_f32 v52, v62, v63
	ds_write2_b64 v92, v[50:51], v[52:53] offset0:96 offset1:176
	global_load_dwordx4 v[50:53], v[70:71], off offset:896
	global_load_dwordx4 v[54:57], v[72:73], off offset:896
	global_load_dwordx4 v[58:61], v[76:77], off offset:896
	global_load_dwordx4 v[62:65], v[74:75], off offset:896
	s_nop 0
	global_load_dword v76, v[68:69], off offset:1792
	global_load_dword v77, v[68:69], off offset:1536
	global_load_dword v93, v[68:69], off offset:1280
	global_load_dword v102, v[68:69], off offset:1024
	global_load_dword v103, v[68:69], off offset:768
	global_load_dword v104, v[68:69], off offset:512
	global_load_dword v105, v[68:69], off offset:256
	global_load_dword v106, v[68:69], off
	s_waitcnt lgkmcnt(0)
	s_barrier
	ds_read_b128 v[68:71], v89 offset:2560
	ds_read_b128 v[72:75], v88 offset:4096
	ds_read_b128 v[94:97], v89 offset:2592
	ds_read_b128 v[98:101], v88 offset:5120
	s_waitcnt lgkmcnt(2)
	v_mfma_f32_32x32x16_f16 v[18:33], v[68:71], v[72:75], v[18:33]
	s_waitcnt lgkmcnt(0)
	v_mfma_f32_32x32x16_f16 v[2:17], v[68:71], v[98:101], v[2:17]
	ds_read_b128 v[68:71], v88 offset:6144
	ds_read_b128 v[72:75], v88 offset:7168
	s_waitcnt vmcnt(12)
	s_waitcnt lgkmcnt(1)
	v_mfma_f32_32x32x16_f16 v[18:33], v[94:97], v[68:71], v[18:33]
	v_mov_b32_e32 v68, v37
	v_mov_b32_e32 v69, v39
	v_mov_b32_e32 v70, v36
	v_mov_b32_e32 v71, v38
	v_cvt_pk_f16_f32 v39, v112, v111
	v_cvt_pk_f16_f32 v38, v114, v113
	s_waitcnt lgkmcnt(0)
	v_mfma_f32_32x32x16_f16 v[2:17], v[94:97], v[72:75], v[2:17]
	v_cvt_pk_f16_f32 v37, v116, v115
	v_cvt_pk_f16_f32 v36, v118, v117
	ds_write_b128 v87, v[36:39]
	v_cvt_pk_f16_f32 v37, v70, v68
	v_cvt_pk_f16_f32 v36, v34, v35
	v_cvt_pk_f16_f32 v35, v40, v41
	v_cvt_pk_f16_f32 v34, v71, v69
	ds_write2_b64 v90, v[36:37], v[34:35] offset1:80
	v_cvt_pk_f16_f32 v35, v44, v45
	v_cvt_pk_f16_f32 v34, v42, v43
	v_cvt_pk_f16_f32 v37, v48, v49
	v_cvt_pk_f16_f32 v36, v46, v47
	ds_write2_b64 v90, v[34:35], v[36:37] offset0:160 offset1:240
	s_waitcnt lgkmcnt(0)
	s_barrier
	ds_read_b128 v[34:37], v89
	ds_read_b128 v[38:41], v88
	ds_read_b128 v[42:45], v89 offset:32
	ds_read_b128 v[46:49], v88 offset:1024
	s_waitcnt lgkmcnt(2)
	v_mfma_f32_32x32x16_f16 v[18:33], v[34:37], v[38:41], v[18:33]
	s_waitcnt lgkmcnt(0)
	v_mfma_f32_32x32x16_f16 v[2:17], v[34:37], v[46:49], v[2:17]
	ds_read_b128 v[34:37], v88 offset:2048
	ds_read_b128 v[38:41], v88 offset:3072
	s_waitcnt vmcnt(0)
	s_waitcnt lgkmcnt(1)
	v_mfma_f32_32x32x16_f16 v[18:33], v[42:45], v[34:37], v[18:33]
	v_mov_b32_e32 v46, v58
	v_mov_b32_e32 v47, v65
	v_mov_b32_e32 v48, v60
	v_mov_b32_e32 v49, v62
	v_cvt_pk_f16_f32 v37, v77, v76
	v_cvt_pk_f16_f32 v36, v102, v93
	v_cvt_pk_f16_f32 v35, v104, v103
	s_waitcnt lgkmcnt(0)
	v_mfma_f32_32x32x16_f16 v[2:17], v[42:45], v[38:41], v[2:17]
	v_mov_b32_e32 v38, v50
	v_mov_b32_e32 v39, v57
	v_mov_b32_e32 v40, v52
	v_mov_b32_e32 v41, v54
	v_mov_b32_e32 v42, v56
	v_mov_b32_e32 v43, v51
	v_mov_b32_e32 v44, v61
	v_mov_b32_e32 v45, v63
	v_cvt_pk_f16_f32 v34, v106, v105
	ds_write_b128 v87, v[34:37] offset:4096
	v_cvt_pk_f16_f32 v35, v40, v53
	v_cvt_pk_f16_f32 v34, v38, v43
	v_cvt_pk_f16_f32 v37, v42, v39
	v_cvt_pk_f16_f32 v36, v41, v55
	ds_write2_b64 v91, v[34:35], v[36:37] offset0:64 offset1:144
	v_cvt_pk_f16_f32 v35, v48, v44
	v_cvt_pk_f16_f32 v34, v46, v59
	v_cvt_pk_f16_f32 v37, v64, v47
	v_cvt_pk_f16_f32 v36, v49, v45
	ds_write2_b64 v92, v[34:35], v[36:37] offset0:96 offset1:176
	s_waitcnt lgkmcnt(0)
	s_barrier
	ds_read_b128 v[34:37], v89 offset:2560
	ds_read_b128 v[38:41], v88 offset:4096
	ds_read_b128 v[42:45], v89 offset:2592
	ds_read_b128 v[46:49], v88 offset:5120
	s_waitcnt lgkmcnt(2)
	v_mfma_f32_32x32x16_f16 v[18:33], v[34:37], v[38:41], v[18:33]
	s_waitcnt lgkmcnt(0)
	v_mfma_f32_32x32x16_f16 v[2:17], v[34:37], v[46:49], v[2:17]
	ds_read_b128 v[34:37], v88 offset:6144
	ds_read_b128 v[38:41], v88 offset:7168
	s_waitcnt lgkmcnt(0)
	s_barrier
	v_mfma_f32_32x32x16_f16 v[18:33], v[42:45], v[34:37], v[18:33]
	v_mfma_f32_32x32x16_f16 v[2:17], v[42:45], v[38:41], v[2:17]
	s_and_saveexec_b64 s[4:5], s[2:3]
	s_cbranch_execz .LBB0_2
	v_lshl_or_b32 v34, v85, 13, v66
	s_nop 7
	ds_write2st64_b32 v34, v18, v19 offset1:1
	ds_write2st64_b32 v34, v20, v21 offset0:2 offset1:3
	ds_write2st64_b32 v34, v22, v23 offset0:4 offset1:5
	ds_write2st64_b32 v34, v24, v25 offset0:6 offset1:7
	ds_write2st64_b32 v34, v26, v27 offset0:8 offset1:9
	ds_write2st64_b32 v34, v28, v29 offset0:10 offset1:11
	ds_write2st64_b32 v34, v30, v31 offset0:12 offset1:13
	ds_write2st64_b32 v34, v32, v33 offset0:14 offset1:15
	ds_write2st64_b32 v34, v2, v3 offset0:16 offset1:17
	ds_write2st64_b32 v34, v4, v5 offset0:18 offset1:19
	ds_write2st64_b32 v34, v6, v7 offset0:20 offset1:21
	ds_write2st64_b32 v34, v8, v9 offset0:22 offset1:23
	ds_write2st64_b32 v34, v10, v11 offset0:24 offset1:25
	ds_write2st64_b32 v34, v12, v13 offset0:26 offset1:27
	ds_write2st64_b32 v34, v14, v15 offset0:28 offset1:29
	ds_write2st64_b32 v34, v16, v17 offset0:30 offset1:31
.LBB0_2:
	s_or_b64 exec, exec, s[4:5]
	s_waitcnt lgkmcnt(0)
	s_barrier
	s_and_saveexec_b64 s[2:3], vcc
	s_cbranch_execz .LBB0_7
	v_lshl_or_b32 v38, v85, 13, v66
	ds_read2st64_b32 v[34:35], v38 offset1:1
	ds_read2st64_b32 v[36:37], v38 offset0:2 offset1:3
	ds_read2st64_b32 v[54:55], v38 offset0:6 offset1:7
	ds_read2st64_b32 v[56:57], v38 offset0:4 offset1:5
	ds_read2st64_b32 v[58:59], v38 offset0:8 offset1:9
	ds_read2st64_b32 v[60:61], v38 offset0:10 offset1:11
	ds_read2st64_b32 v[62:63], v38 offset0:12 offset1:13
	ds_read2st64_b32 v[64:65], v38 offset0:14 offset1:15
	s_mov_b64 s[2:3], s[12:13]
	ds_read2st64_b32 v[68:69], v38 offset0:16 offset1:17
	ds_read2st64_b32 v[52:53], v38 offset0:18 offset1:19
	ds_read2st64_b32 v[48:49], v38 offset0:20 offset1:21
	ds_read2st64_b32 v[50:51], v38 offset0:22 offset1:23
	ds_read2st64_b32 v[46:47], v38 offset0:24 offset1:25
	ds_read2st64_b32 v[44:45], v38 offset0:26 offset1:27
	ds_read2st64_b32 v[40:41], v38 offset0:28 offset1:29
	ds_read2st64_b32 v[42:43], v38 offset0:30 offset1:31
	s_waitcnt lgkmcnt(0)
	v_add_f32_e32 v66, v18, v34
	v_add_f32_e32 v58, v26, v58
	v_add_f32_e32 v26, v33, v65
	v_add_f32_e32 v65, v2, v68
	v_cvt_f16_f32_e32 v2, v66
	v_lshlrev_b32_e32 v38, 4, v84
	v_mov_b32_e32 v39, 0
	v_mov_b32_e32 v34, v35
	v_mov_b32_e32 v35, v36
	v_mov_b32_e32 v18, v19
	v_mov_b32_e32 v19, v20
	v_lshl_add_u64 v[72:73], s[2:3], 0, v[38:39]
	v_pk_add_f32 v[38:39], v[18:19], v[34:35]
	v_mov_b32_e32 v34, v37
	v_mov_b32_e32 v35, v56
	v_mov_b32_e32 v20, v21
	v_mov_b32_e32 v21, v22
	v_add_f32_e32 v46, v10, v46
	v_add_f32_e32 v10, v17, v43
	v_cvt_pk_f16_f32 v17, v38, v39
	v_pk_add_f32 v[34:35], v[20:21], v[34:35]
	v_add_f32_e32 v74, v25, v55
	v_pack_b32_f16 v18, v2, v17
	v_cvt_pk_f16_f32 v2, v34, v35
	v_add_f32_e32 v51, v9, v51
	v_ashrrev_i32_e32 v9, 4, v1
	s_mul_i32 s4, s8, 0xc0
	v_alignbit_b32 v19, v2, v17, 16
	v_cvt_f16_f32_e32 v17, v74
	v_add_u32_e32 v70, s4, v9
	v_mov_b32_e32 v20, v57
	v_mov_b32_e32 v21, v54
	v_mov_b32_e32 v22, v23
	v_mov_b32_e32 v23, v24
	v_pk_add_f32 v[36:37], v[22:23], v[20:21]
	v_ashrrev_i32_e32 v71, 31, v70
	v_cvt_pk_f16_f32 v21, v36, v37
	v_lshlrev_b64 v[22:23], 11, v[70:71]
	v_alignbit_b32 v20, v21, v2, 16
	v_alignbit_b32 v21, v17, v21, 16
	v_lshl_add_u64 v[54:55], v[72:73], 0, v[22:23]
	v_cvt_f16_f32_e32 v2, v58
	global_store_dwordx4 v[54:55], v[18:21], off
	v_mov_b32_e32 v22, v31
	v_mov_b32_e32 v23, v32
	v_mov_b32_e32 v18, v59
	v_mov_b32_e32 v19, v60
	v_mov_b32_e32 v20, v27
	v_mov_b32_e32 v21, v28
	v_pk_add_f32 v[24:25], v[20:21], v[18:19]
	v_mov_b32_e32 v18, v61
	v_mov_b32_e32 v19, v62
	v_mov_b32_e32 v20, v29
	v_mov_b32_e32 v21, v30
	v_cvt_pk_f16_f32 v17, v24, v25
	v_pk_add_f32 v[20:21], v[20:21], v[18:19]
	v_pack_b32_f16 v28, v2, v17
	v_cvt_pk_f16_f32 v2, v20, v21
	v_alignbit_b32 v29, v2, v17, 16
	v_cvt_f16_f32_e32 v17, v26
	v_mov_b32_e32 v18, v63
	v_mov_b32_e32 v19, v64
	v_pk_add_f32 v[22:23], v[22:23], v[18:19]
	s_nop 0
	v_cvt_pk_f16_f32 v18, v22, v23
	v_alignbit_b32 v30, v18, v2, 16
	v_alignbit_b32 v31, v17, v18, 16
	v_or_b32_e32 v18, 1, v70
	v_ashrrev_i32_e32 v19, 31, v18
	v_lshlrev_b64 v[18:19], 11, v[18:19]
	v_lshl_add_u64 v[18:19], v[72:73], 0, v[18:19]
	v_cvt_f16_f32_e32 v17, v65
	global_store_dwordx4 v[18:19], v[28:31], off
	v_mov_b32_e32 v2, v3
	v_mov_b32_e32 v3, v4
	v_mov_b32_e32 v28, v69
	v_mov_b32_e32 v29, v52
	v_mov_b32_e32 v30, v53
	v_mov_b32_e32 v31, v48
	v_mov_b32_e32 v4, v5
	v_mov_b32_e32 v5, v6
	v_mov_b32_e32 v6, v7
	v_mov_b32_e32 v7, v8
	v_cvt_f16_f32_e32 v8, v51
	v_pk_add_f32 v[28:29], v[2:3], v[28:29]
	v_pk_add_f32 v[30:31], v[4:5], v[30:31]
	v_mov_b32_e32 v4, v49
	v_mov_b32_e32 v5, v50
	v_cvt_pk_f16_f32 v3, v28, v29
	v_pk_add_f32 v[6:7], v[6:7], v[4:5]
	v_pack_b32_f16 v2, v17, v3
	v_cvt_pk_f16_f32 v17, v30, v31
	v_cvt_pk_f16_f32 v5, v6, v7
	v_alignbit_b32 v3, v17, v3, 16
	v_alignbit_b32 v4, v5, v17, 16
	v_alignbit_b32 v5, v8, v5, 16
	global_store_dwordx4 v[54:55], v[2:5], off offset:1024
	v_cvt_f16_f32_e32 v8, v46
	v_mul_f32_e32 v17, v82, v28
	v_mov_b32_e32 v2, v47
	v_mov_b32_e32 v3, v44
	v_mov_b32_e32 v4, v11
	v_mov_b32_e32 v5, v12
	v_pk_add_f32 v[32:33], v[4:5], v[2:3]
	v_mov_b32_e32 v5, v40
	v_mov_b32_e32 v12, v13
	v_mov_b32_e32 v13, v14
	v_mov_b32_e32 v40, v41
	v_mov_b32_e32 v41, v42
	v_mov_b32_e32 v14, v15
	v_mov_b32_e32 v15, v16
	v_mbcnt_lo_u32_b32 v42, -1, 0
	v_cvt_pk_f16_f32 v3, v32, v33
	v_mov_b32_e32 v4, v45
	v_pk_add_f32 v[14:15], v[14:15], v[40:41]
	v_mul_f32_e32 v41, v83, v32
	v_mul_f32_e32 v32, v82, v32
	v_mbcnt_hi_u32_b32 v42, -1, v42
	v_pk_add_f32 v[12:13], v[12:13], v[4:5]
	v_fmac_f32_e32 v41, v80, v24
	v_fmac_f32_e32 v32, v81, v24
	v_mul_f32_e32 v24, v83, v33
	v_mul_f32_e32 v33, v82, v33
	v_and_b32_e32 v43, 64, v42
	v_cvt_pk_f16_f32 v4, v12, v13
	v_fmac_f32_e32 v24, v80, v25
	v_fmac_f32_e32 v33, v81, v25
	v_mul_f32_e32 v25, v83, v12
	v_mul_f32_e32 v12, v82, v12
	v_add_u32_e32 v43, 64, v43
	v_xor_b32_e32 v45, 16, v42
	v_pack_b32_f16 v2, v8, v3
	v_mul_f32_e32 v8, v83, v65
	v_mul_f32_e32 v11, v82, v65
	v_mul_f32_e32 v16, v83, v28
	v_fmac_f32_e32 v25, v80, v20
	v_fmac_f32_e32 v12, v81, v20
	v_mul_f32_e32 v20, v83, v13
	v_mul_f32_e32 v13, v82, v13
	v_and_b32_e32 v44, 16, v0
	v_cmp_lt_i32_e32 vcc, v45, v43
	v_cvt_pk_f16_f32 v5, v14, v15
	v_fmac_f32_e32 v8, v80, v66
	v_fmac_f32_e32 v11, v81, v66
	v_fmac_f32_e32 v16, v80, v38
	v_fmac_f32_e32 v17, v81, v38
	v_mul_f32_e32 v27, v83, v29
	v_mul_f32_e32 v28, v82, v29
	v_fmac_f32_e32 v20, v80, v21
	v_fmac_f32_e32 v13, v81, v21
	v_mul_f32_e32 v21, v83, v14
	v_mul_f32_e32 v14, v82, v14
	v_cndmask_b32_e32 v45, v42, v45, vcc
	v_cmp_eq_u32_e32 vcc, 0, v44
	v_fmac_f32_e32 v27, v80, v39
	v_fmac_f32_e32 v28, v81, v39
	v_mul_f32_e32 v29, v83, v30
	v_mul_f32_e32 v30, v82, v30
	v_fmac_f32_e32 v21, v80, v22
	v_fmac_f32_e32 v14, v81, v22
	v_mul_f32_e32 v22, v83, v15
	v_mul_f32_e32 v15, v82, v15
	v_lshlrev_b32_e32 v45, 2, v45
	v_cndmask_b32_e32 v44, v8, v11, vcc
	v_cndmask_b32_e32 v8, v11, v8, vcc
	v_cndmask_b32_e32 v11, v16, v17, vcc
	v_fmac_f32_e32 v29, v80, v34
	v_fmac_f32_e32 v30, v81, v34
	v_mul_f32_e32 v39, v83, v46
	v_mul_f32_e32 v40, v82, v46
	v_fmac_f32_e32 v22, v80, v23
	v_fmac_f32_e32 v15, v81, v23
	v_mul_f32_e32 v23, v83, v10
	v_mul_f32_e32 v46, v82, v10
	v_cndmask_b32_e32 v16, v17, v16, vcc
	ds_bpermute_b32 v11, v45, v11
	v_cndmask_b32_e32 v17, v27, v28, vcc
	v_fmac_f32_e32 v23, v80, v26
	v_fmac_f32_e32 v46, v81, v26
	ds_bpermute_b32 v17, v45, v17
	v_cndmask_b32_e32 v26, v29, v30, vcc
	ds_bpermute_b32 v26, v45, v26
	v_mul_f32_e32 v34, v83, v31
	v_mul_f32_e32 v31, v82, v31
	v_fmac_f32_e32 v34, v80, v35
	v_fmac_f32_e32 v31, v81, v35
	v_mul_f32_e32 v35, v83, v6
	v_mul_f32_e32 v6, v82, v6
	s_waitcnt lgkmcnt(2)
	v_add_f32_e32 v11, v16, v11
	v_cndmask_b32_e32 v16, v28, v27, vcc
	v_fmac_f32_e32 v35, v80, v36
	v_fmac_f32_e32 v6, v81, v36
	v_mul_f32_e32 v36, v83, v7
	v_mul_f32_e32 v7, v82, v7
	s_waitcnt lgkmcnt(1)
	v_add_f32_e32 v16, v16, v17
	v_cndmask_b32_e32 v17, v30, v29, vcc
	v_fmac_f32_e32 v36, v80, v37
	v_fmac_f32_e32 v7, v81, v37
	s_waitcnt lgkmcnt(0)
	v_add_f32_e32 v17, v17, v26
	v_cndmask_b32_e32 v26, v34, v31, vcc
	ds_bpermute_b32 v26, v45, v26
	v_cndmask_b32_e32 v29, v36, v7, vcc
	ds_bpermute_b32 v29, v45, v29
	v_mul_f32_e32 v37, v83, v51
	v_mul_f32_e32 v38, v82, v51
	v_fmac_f32_e32 v37, v80, v74
	v_fmac_f32_e32 v38, v81, v74
	v_cndmask_b32_e32 v27, v31, v34, vcc
	v_cndmask_b32_e32 v28, v35, v6, vcc
	v_fmac_f32_e32 v39, v80, v58
	v_fmac_f32_e32 v40, v81, v58
	ds_bpermute_b32 v28, v45, v28
	s_waitcnt lgkmcnt(2)
	v_add_f32_e32 v26, v27, v26
	v_cndmask_b32_e32 v7, v7, v36, vcc
	v_cndmask_b32_e32 v27, v37, v38, vcc
	s_waitcnt lgkmcnt(1)
	v_add_f32_e32 v7, v7, v29
	ds_bpermute_b32 v27, v45, v27
	v_cndmask_b32_e32 v29, v39, v40, vcc
	ds_bpermute_b32 v29, v45, v29
	v_cndmask_b32_e32 v6, v6, v35, vcc
	s_waitcnt lgkmcnt(2)
	v_add_f32_e32 v6, v6, v28
	v_cndmask_b32_e32 v28, v38, v37, vcc
	s_waitcnt lgkmcnt(1)
	v_add_f32_e32 v27, v28, v27
	v_cndmask_b32_e32 v28, v40, v39, vcc
	v_cndmask_b32_e32 v30, v41, v32, vcc
	s_waitcnt lgkmcnt(0)
	v_add_f32_e32 v28, v28, v29
	v_cndmask_b32_e32 v29, v32, v41, vcc
	v_cndmask_b32_e32 v32, v20, v13, vcc
	v_cndmask_b32_e32 v13, v13, v20, vcc
	v_cndmask_b32_e32 v20, v21, v14, vcc
	v_cndmask_b32_e32 v14, v14, v21, vcc
	v_cndmask_b32_e32 v21, v22, v15, vcc
	ds_bpermute_b32 v30, v45, v30
	ds_bpermute_b32 v20, v45, v20
	ds_bpermute_b32 v21, v45, v21
	ds_bpermute_b32 v44, v45, v44
	v_cndmask_b32_e32 v15, v15, v22, vcc
	v_xor_b32_e32 v22, 8, v42
	s_waitcnt lgkmcnt(3)
	v_add_f32_e32 v29, v29, v30
	v_cndmask_b32_e32 v30, v24, v33, vcc
	v_cndmask_b32_e32 v24, v33, v24, vcc
	v_cndmask_b32_e32 v31, v25, v12, vcc
	v_cndmask_b32_e32 v12, v12, v25, vcc
	v_cndmask_b32_e32 v25, v23, v46, vcc
	s_waitcnt lgkmcnt(2)
	v_add_f32_e32 v14, v14, v20
	s_waitcnt lgkmcnt(1)
	v_add_f32_e32 v15, v15, v21
	v_cndmask_b32_e32 v20, v46, v23, vcc
	v_and_b32_e32 v21, 8, v0
	v_cmp_lt_i32_e32 vcc, v22, v43
	s_waitcnt lgkmcnt(0)
	v_add_f32_e32 v8, v8, v44
	ds_bpermute_b32 v31, v45, v31
	v_cndmask_b32_e32 v22, v42, v22, vcc
	v_cmp_eq_u32_e32 vcc, 0, v21
	v_lshlrev_b32_e32 v22, 2, v22
	ds_bpermute_b32 v32, v45, v32
	v_cndmask_b32_e32 v21, v8, v28, vcc
	s_nop 1
	v_mov_b32_dpp v21, v21 row_ror:8 row_mask:0xf bank_mask:0xf
	v_cndmask_b32_e32 v23, v11, v29, vcc
	ds_bpermute_b32 v30, v45, v30
	s_nop 1
	v_mov_b32_dpp v23, v23 row_ror:8 row_mask:0xf bank_mask:0xf
	s_waitcnt lgkmcnt(2)
	v_add_f32_e32 v12, v12, v31
	ds_bpermute_b32 v25, v45, v25
	v_cndmask_b32_e32 v8, v28, v8, vcc
	s_waitcnt lgkmcnt(2)
	v_add_f32_e32 v13, v13, v32
	s_waitcnt lgkmcnt(2)
	v_add_f32_e32 v8, v8, v21
	v_cndmask_b32_e32 v21, v17, v12, vcc
	v_cndmask_b32_e32 v12, v12, v17, vcc
	s_nop 1
	v_mov_b32_dpp v17, v21 row_ror:8 row_mask:0xf bank_mask:0xf
	v_cndmask_b32_e32 v21, v26, v13, vcc
	v_cndmask_b32_e32 v11, v29, v11, vcc
	s_nop 1
	v_mov_b32_dpp v21, v21 row_ror:8 row_mask:0xf bank_mask:0xf
	s_waitcnt lgkmcnt(1)
	v_add_f32_e32 v24, v24, v30
	s_waitcnt lgkmcnt(1)
	v_add_f32_e32 v11, v11, v23
	v_cndmask_b32_e32 v23, v6, v14, vcc
	s_waitcnt lgkmcnt(0)
	v_add_f32_e32 v20, v20, v25
	v_cndmask_b32_e32 v25, v16, v24, vcc
	s_nop 1
	v_mov_b32_dpp v23, v23 row_ror:8 row_mask:0xf bank_mask:0xf
	v_cndmask_b32_e32 v6, v14, v6, vcc
	v_cndmask_b32_e32 v14, v7, v15, vcc
	s_nop 1
	v_mov_b32_dpp v25, v25 row_ror:8 row_mask:0xf bank_mask:0xf
	s_nop 1
	v_mov_b32_dpp v14, v14 row_ror:8 row_mask:0xf bank_mask:0xf
	v_cndmask_b32_e32 v13, v13, v26, vcc
	v_cndmask_b32_e32 v7, v15, v7, vcc
	v_cndmask_b32_e32 v15, v27, v20, vcc
	s_waitcnt lgkmcnt(0)
	v_add_f32_e32 v13, v13, v21
	s_nop 1
	v_mov_b32_dpp v15, v15 row_ror:8 row_mask:0xf bank_mask:0xf
	v_xor_b32_e32 v21, 4, v42
	v_add_f32_e32 v12, v12, v17
	v_and_b32_e32 v17, 4, v0
	v_cmp_lt_i32_e64 s[2:3], v21, v43
	v_cndmask_b32_e32 v16, v24, v16, vcc
	s_waitcnt lgkmcnt(0)
	v_add_f32_e32 v6, v6, v23
	v_cndmask_b32_e64 v21, v42, v21, s[2:3]
	v_cmp_eq_u32_e64 s[2:3], 0, v17
	s_waitcnt lgkmcnt(0)
	v_add_f32_e32 v16, v16, v25
	v_lshlrev_b32_e32 v21, 2, v21
	v_cndmask_b32_e64 v17, v8, v13, s[2:3]
	s_waitcnt lgkmcnt(0)
	v_add_f32_e32 v7, v7, v14
	v_cndmask_b32_e64 v8, v13, v8, s[2:3]
	v_cndmask_b32_e64 v13, v11, v6, s[2:3]
	v_cndmask_b32_e32 v14, v20, v27, vcc
	v_cndmask_b32_e64 v6, v6, v11, s[2:3]
	s_nop 1
	v_mov_b32_dpp v11, v13 row_half_mirror row_mask:0xf bank_mask:0xf
	s_nop 1
	v_mov_b32_dpp v11, v11 quad_perm:[3,2,1,0] row_mask:0xf bank_mask:0xf
	v_cndmask_b32_e64 v13, v16, v7, s[2:3]
	s_waitcnt lgkmcnt(0)
	v_add_f32_e32 v14, v14, v15
	s_nop 1
	v_mov_b32_dpp v13, v13 row_half_mirror row_mask:0xf bank_mask:0xf
	s_nop 1
	v_mov_b32_dpp v13, v13 quad_perm:[3,2,1,0] row_mask:0xf bank_mask:0xf
	v_cndmask_b32_e64 v15, v12, v14, s[2:3]
	s_nop 1
	v_mov_b32_dpp v17, v17 row_half_mirror row_mask:0xf bank_mask:0xf
	s_nop 1
	v_mov_b32_dpp v17, v17 quad_perm:[3,2,1,0] row_mask:0xf bank_mask:0xf
	s_nop 1
	v_mov_b32_dpp v15, v15 row_half_mirror row_mask:0xf bank_mask:0xf
	s_nop 1
	v_mov_b32_dpp v15, v15 quad_perm:[3,2,1,0] row_mask:0xf bank_mask:0xf
	v_cndmask_b32_e64 v7, v7, v16, s[2:3]
	s_waitcnt lgkmcnt(0)
	v_add_f32_e32 v7, v7, v13
	v_xor_b32_e32 v13, 2, v42
	v_add_f32_e32 v6, v6, v11
	v_cndmask_b32_e64 v11, v14, v12, s[2:3]
	v_and_b32_e32 v12, 2, v0
	v_cmp_lt_i32_e32 vcc, v13, v43
	s_waitcnt lgkmcnt(0)
	v_add_f32_e32 v8, v8, v17
	s_waitcnt lgkmcnt(0)
	v_add_f32_e32 v11, v11, v15
	v_cndmask_b32_e32 v13, v42, v13, vcc
	v_cmp_eq_u32_e32 vcc, 0, v12
	v_lshlrev_b32_e32 v13, 2, v13
	v_cvt_f16_f32_e32 v10, v10
	v_cndmask_b32_e32 v12, v8, v7, vcc
	v_cndmask_b32_e32 v14, v6, v11, vcc
	s_nop 1
	v_mov_b32_dpp v12, v12 quad_perm:[2,3,0,1] row_mask:0xf bank_mask:0xf
	s_nop 1
	v_mov_b32_dpp v13, v14 quad_perm:[2,3,0,1] row_mask:0xf bank_mask:0xf
	v_cndmask_b32_e32 v6, v11, v6, vcc
	v_xor_b32_e32 v11, 1, v42
	v_cndmask_b32_e32 v7, v7, v8, vcc
	v_and_b32_e32 v8, 1, v0
	v_cmp_lt_i32_e32 vcc, v11, v43
	s_waitcnt lgkmcnt(0)
	v_add_f32_e32 v7, v7, v12
	s_waitcnt lgkmcnt(0)
	v_add_f32_e32 v6, v6, v13
	v_cndmask_b32_e32 v11, v42, v11, vcc
	v_cmp_eq_u32_e32 vcc, 0, v8
	v_lshlrev_b32_e32 v11, 2, v11
	v_alignbit_b32 v3, v4, v3, 16
	v_cndmask_b32_e32 v8, v7, v6, vcc
	s_nop 1
	v_mov_b32_dpp v8, v8 quad_perm:[1,0,3,2] row_mask:0xf bank_mask:0xf
	v_alignbit_b32 v4, v5, v4, 16
	v_alignbit_b32 v5, v10, v5, 16
	global_store_dwordx4 v[18:19], v[2:5], off offset:1024
	s_nop 1
	v_cndmask_b32_e32 v2, v6, v7, vcc
	s_waitcnt lgkmcnt(0)
	v_add_f32_e32 v2, v2, v8
	v_cmp_lt_u32_e32 vcc, 15, v79
	s_and_saveexec_b64 s[2:3], vcc
	s_xor_b64 s[2:3], exec, s[2:3]
	s_cbranch_execz .LBB0_5
	v_mul_f32_e32 v1, 0x3fb8aa3b, v2
	v_mul_f32_e32 v2, 0x3e4ccccd, v2
	s_lshr_b32 s6, s8, 2
	v_add_u32_e32 v0, -16, v79
	v_exp_f32_e32 v1, v1
	v_mul_f32_e32 v2, 0x3fb8aa3b, v2
	v_lshrrev_b32_e32 v0, 3, v0
	s_mulk_i32 s6, 0xc0
	v_exp_f32_e32 v2, v2
	s_mov_b64 s[4:5], s[14:15]
	v_add_u32_e32 v0, s6, v0
	s_lshl_b32 s6, s8, 1
	v_add_lshl_u32 v0, v0, v9, 3
	s_and_b32 s6, s6, 6
	v_or3_b32 v0, v0, s6, v67
	v_cvt_f16_f32_e32 v3, v1
	v_lshl_or_b32 v0, v0, 4, v78
	v_cvt_f16_f32_e32 v2, v2
	v_ashrrev_i32_e32 v1, 31, v0
	s_waitcnt lgkmcnt(0)
	v_lshl_add_u64 v[0:1], v[0:1], 1, s[4:5]
	global_store_short v[0:1], v3, off
	global_store_short v[0:1], v2, off offset:16
.LBB0_5:
	s_andn2_saveexec_b64 s[2:3], s[2:3]
	s_cbranch_execz .LBB0_7
	v_mul_f32_e32 v2, 0xbf4ccccd, v2
	v_mul_f32_e32 v2, 0x3fb8aa3b, v2
	v_exp_f32_e32 v2, v2
	v_lshlrev_b32_e32 v3, 1, v0
	s_mov_b64 s[0:1], s[16:17]
	v_and_b32_e32 v3, 24, v3
	v_and_or_b32 v0, v0, 3, v3
	v_lshlrev_b32_e32 v3, 2, v67
	s_mul_i32 s2, s8, 0xc00
	v_cvt_f16_f32_e32 v2, v2
	v_or3_b32 v0, v0, v3, s2
	v_add_u32_e32 v0, v0, v1
	v_ashrrev_i32_e32 v1, 31, v0
	s_waitcnt lgkmcnt(0)
	v_lshl_add_u64 v[0:1], v[0:1], 1, s[0:1]
	global_store_short v[0:1], v2, off

_Z10epi_kernelPKDF16_PKfS2_S2_S2_S2_Pf:
	s_load_dwordx8 s[4:11], s[0:1], 0x0
	s_load_dwordx2 s[56:57], s[0:1], 0x20
	s_load_dwordx2 s[58:59], s[0:1], 0x28
	s_load_dwordx2 s[60:61], s[0:1], 0x30
	s_load_dwordx2 s[20:21], s[0:1], 0x20
	s_load_dwordx2 s[22:23], s[0:1], 0x30
	v_and_b32_e32 v55, 15, v0
	v_mov_b32_e32 v99, 0
	v_bfe_u32 v70, v0, 4, 2
	v_and_b32_e32 v2, 0xc0, v0
	v_lshl_or_b32 v16, v70, 3, v2
	v_lshlrev_b32_e32 v2, 10, v55
	v_mov_b32_e32 v3, v99
	v_lshrrev_b32_e32 v1, 6, v0
	s_waitcnt lgkmcnt(0)
	s_mov_b32 s30, 0
	v_readfirstlane_b32 s24, v1
	s_cmp_lg_u32 s2, 0xbf
	s_cbranch_scc1 .Lk3_l1skipB
	s_cmp_lg_u32 s24, 3
	s_cbranch_scc1 .Lk3_l1skipB
	s_mov_b32 s30, 1
	v_and_b32_e32 v124, 63, v0
	v_lshlrev_b32_e32 v124, 2, v124
	global_load_dword v112, v124, s[20:21]
	global_load_dword v113, v124, s[20:21] offset:256
	global_load_dword v114, v124, s[20:21] offset:512
	global_load_dword v115, v124, s[20:21] offset:768
	global_load_dword v116, v124, s[20:21] offset:1024
	global_load_dword v117, v124, s[20:21] offset:1280
	global_load_dword v118, v124, s[20:21] offset:1536
	global_load_dword v119, v124, s[20:21] offset:1792
	global_load_dword v120, v124, s[20:21] offset:2048
	global_load_dword v121, v124, s[20:21] offset:2304
	global_load_dword v122, v124, s[20:21] offset:2560
	global_load_dword v123, v124, s[20:21] offset:2816
.Lk3_l1skipB:
	v_lshl_add_u64 v[2:3], s[8:9], 0, v[2:3]
	v_lshlrev_b32_e32 v4, 2, v16
	v_mov_b32_e32 v5, v99
	s_bfe_i32 s16, s2, 0x1a0002
	v_lshl_add_u64 v[2:3], v[2:3], 0, v[4:5]
	v_lshlrev_b32_e32 v4, 2, v1
	s_mul_i32 s15, s16, 48
	v_lshl_add_u64 v[52:53], s[6:7], 0, v[4:5]
	s_mul_hi_i32 s6, s15, 0x4bda12f7
	s_lshr_b32 s7, s6, 31
	s_ashr_i32 s6, s6, 3
	s_add_i32 s6, s6, s7
	s_add_i32 s7, s15, 47
	s_mul_hi_i32 s7, s7, 0x4bda12f7
	s_lshr_b32 s8, s7, 31
	s_ashr_i32 s7, s7, 3
	s_lshl_b32 s3, s2, 4
	s_add_i32 s8, s7, s8
	s_and_b32 s14, s3, 48
	s_sub_i32 s7, s8, s6
	s_cmp_eq_u32 s7, 2
	s_mul_i32 s17, s6, 27
	s_cselect_b64 s[12:13], -1, 0
	s_lshl_b32 s9, s6, 1
	s_mul_hi_i32 s6, s17, 0x2aaaaaab
	s_lshr_b32 s7, s6, 31
	s_ashr_i32 s6, s6, 3
	s_add_i32 s6, s6, s7
	s_cmp_lg_u32 s6, s16
	s_cselect_b64 s[6:7], -1, 0
	s_add_i32 s17, s17, 27
	v_cndmask_b32_e64 v4, 0, 1, s[6:7]
	s_mul_hi_i32 s6, s17, 0x2aaaaaab
	s_lshr_b32 s7, s6, 31
	s_ashr_i32 s6, s6, 3
	s_add_i32 s6, s6, s7
	s_cmp_lg_u32 s6, s16
	s_cselect_b64 s[6:7], -1, 0
	v_cndmask_b32_e64 v6, 0, 1, s[6:7]
	v_or_b32_e32 v4, s9, v4
	v_or_b32_e32 v6, s9, v6
	s_lshl_b32 s9, s8, 1
	s_mul_i32 s8, s8, 27
	s_mul_hi_i32 s6, s8, 0x2aaaaaab
	s_lshr_b32 s7, s6, 31
	s_ashr_i32 s6, s6, 3
	s_add_i32 s6, s6, s7
	s_cmp_lg_u32 s6, s16
	s_cselect_b64 s[6:7], -1, 0
	v_cndmask_b32_e64 v8, 0, 1, s[6:7]
	v_ashrrev_i32_e32 v5, 31, v4
	v_add_u32_e32 v6, 2, v6
	v_or_b32_e32 v8, s9, v8
	global_load_dwordx4 v[18:21], v[2:3], off
	v_lshlrev_b64 v[4:5], 6, v[4:5]
	v_ashrrev_i32_e32 v7, 31, v6
	v_ashrrev_i32_e32 v9, 31, v8
	v_or_b32_e32 v4, v4, v55
	v_lshlrev_b64 v[6:7], 6, v[6:7]
	v_lshlrev_b64 v[8:9], 6, v[8:9]
	v_or_b32_e32 v4, s14, v4
	v_or_b32_e32 v6, v6, v55
	v_or_b32_e32 v8, v8, v55
	v_or_b32_e32 v6, s14, v6
	v_or_b32_e32 v8, s14, v8
	v_lshl_add_u64 v[10:11], v[4:5], 4, v[52:53]
	v_lshl_add_u64 v[12:13], v[6:7], 4, v[52:53]
	v_lshl_add_u64 v[14:15], v[8:9], 4, v[52:53]
	global_load_dword v71, v[10:11], off
	global_load_dword v72, v[12:13], off
	global_load_dword v73, v[14:15], off
	global_load_dwordx4 v[30:33], v[2:3], off offset:16
	global_load_dwordx4 v[26:29], v[2:3], off offset:128
	global_load_dwordx4 v[22:25], v[2:3], off offset:144
	v_lshlrev_b32_e32 v2, 1, v16
	v_mov_b32_e32 v3, v99
	v_lshl_add_u64 v[50:51], s[4:5], 0, v[2:3]
	v_lshlrev_b64 v[2:3], 9, v[4:5]
	v_lshl_add_u64 v[64:65], v[50:51], 0, v[2:3]
	v_lshlrev_b64 v[2:3], 9, v[6:7]
	v_lshl_add_u64 v[66:67], v[50:51], 0, v[2:3]
	v_lshlrev_b64 v[2:3], 9, v[8:9]
	global_load_dwordx4 v[34:37], v[64:65], off
	global_load_dwordx4 v[56:59], v[66:67], off
	v_lshl_add_u64 v[68:69], v[50:51], 0, v[2:3]
	global_load_dwordx4 v[60:63], v[68:69], off
	s_mov_b64 s[4:5], s[56:57]
	s_mov_b64 s[6:7], s[58:59]
	s_mov_b64 s[8:9], s[60:61]
	v_mul_u32_u24_e32 v2, 48, v55
	v_lshlrev_b32_e32 v98, 2, v55
	v_lshlrev_b32_e32 v106, 2, v2
	global_load_dword v100, v98, s[10:11]
	s_waitcnt lgkmcnt(0)
	global_load_dword v101, v98, s[6:7]
	global_load_dwordx4 v[2:5], v106, s[4:5] offset:48
	global_load_dwordx4 v[6:9], v106, s[4:5] offset:32
	global_load_dwordx4 v[10:13], v106, s[4:5] offset:16
	global_load_dwordx4 v[14:17], v106, s[4:5]
	global_load_dwordx4 v[46:49], v[64:65], off offset:64
	global_load_dwordx4 v[42:45], v[66:67], off offset:64
	global_load_dwordx4 v[38:41], v[68:69], off offset:64
	v_cndmask_b32_e64 v54, 0, 1.0, s[12:13]
	s_add_i32 s12, s16, 0x60
	s_add_i32 s16, s16, 48
	s_cmp_lg_u32 s30, 1
	s_cbranch_scc1 .Lk3_l1skipC
	s_mov_b64 s[28:29], vcc
	s_waitcnt vmcnt(19)
	v_add_f32_e64 v127, |v112|, |v113|
	v_add_f32_e64 v127, v127, |v114|
	v_add_f32_e64 v127, v127, |v115|
	v_add_f32_e64 v127, v127, |v116|
	v_add_f32_e64 v127, v127, |v117|
	v_add_f32_e64 v127, v127, |v118|
	v_add_f32_e64 v127, v127, |v119|
	v_add_f32_e64 v127, v127, |v120|
	v_add_f32_e64 v127, v127, |v121|
	v_add_f32_e64 v127, v127, |v122|
	v_add_f32_e64 v127, v127, |v123|
	v_xor_b32_e32 v125, 128, v124
	ds_bpermute_b32 v126, v125, v127
	s_waitcnt lgkmcnt(0)
	v_add_f32_e32 v127, v127, v126
	v_xor_b32_e32 v125, 64, v124
	ds_bpermute_b32 v126, v125, v127
	s_waitcnt lgkmcnt(0)
	v_add_f32_e32 v127, v127, v126
	v_xor_b32_e32 v125, 32, v124
	ds_bpermute_b32 v126, v125, v127
	s_waitcnt lgkmcnt(0)
	v_add_f32_e32 v127, v127, v126
	v_xor_b32_e32 v125, 16, v124
	ds_bpermute_b32 v126, v125, v127
	s_waitcnt lgkmcnt(0)
	v_add_f32_e32 v127, v127, v126
	v_xor_b32_e32 v125, 8, v124
	ds_bpermute_b32 v126, v125, v127
	s_waitcnt lgkmcnt(0)
	v_add_f32_e32 v127, v127, v126
	v_xor_b32_e32 v125, 4, v124
	ds_bpermute_b32 v126, v125, v127
	s_waitcnt lgkmcnt(0)
	v_add_f32_e32 v127, v127, v126
	s_mov_b32 s25, 0x44400000
	v_div_scale_f32 v125, s[26:27], s25, s25, v127
	v_rcp_f32_e32 v126, v125
	s_nop 0
	v_fma_f32 v123, -v125, v126, 1.0
	v_fmac_f32_e32 v126, v123, v126
	v_div_scale_f32 v123, vcc, v127, s25, v127
	v_mul_f32_e32 v122, v123, v126
	v_fma_f32 v121, -v125, v122, v123
	v_fmac_f32_e32 v122, v121, v126
	v_fma_f32 v125, -v125, v122, v123
	s_nop 3
	v_div_fmas_f32 v125, v125, v126, v122
	v_div_fixup_f32 v127, v125, s25, v127
	v_mov_b32_e32 v125, 0x30000
	v_cmp_eq_u32_e32 vcc, 0, v124
	s_and_saveexec_b64 s[26:27], vcc
	global_store_dword v125, v127, s[22:23]
	s_mov_b64 exec, s[26:27]
	s_mov_b64 vcc, s[28:29]

	.amdhsa_kernel _Z10epi_kernelPKDF16_PKfS2_S2_S2_S2_Pf
		.amdhsa_group_segment_fixed_size 16192
		.amdhsa_private_segment_fixed_size 0
		.amdhsa_kernarg_size 56
		.amdhsa_user_sgpr_count 2
		.amdhsa_user_sgpr_dispatch_ptr 0
		.amdhsa_user_sgpr_queue_ptr 0
		.amdhsa_user_sgpr_kernarg_segment_ptr 1
		.amdhsa_user_sgpr_dispatch_id 0
		.amdhsa_user_sgpr_kernarg_preload_length 0
		.amdhsa_user_sgpr_kernarg_preload_offset 0
		.amdhsa_user_sgpr_private_segment_size 0
		.amdhsa_uses_dynamic_stack 0
		.amdhsa_enable_private_segment 0
		.amdhsa_system_sgpr_workgroup_id_x 1
		.amdhsa_system_sgpr_workgroup_id_y 0
		.amdhsa_system_sgpr_workgroup_id_z 0
		.amdhsa_system_sgpr_workgroup_info 0
		.amdhsa_system_vgpr_workitem_id 0
		.amdhsa_next_free_vgpr 140
		.amdhsa_next_free_sgpr 64
		.amdhsa_accum_offset 128
		.amdhsa_reserve_vcc 1
		.amdhsa_float_round_mode_32 0
		.amdhsa_float_round_mode_16_64 0
		.amdhsa_float_denorm_mode_32 3
		.amdhsa_float_denorm_mode_16_64 3
		.amdhsa_dx10_clamp 1
		.amdhsa_ieee_mode 1
		.amdhsa_fp16_overflow 0
		.amdhsa_tg_split 0
		.amdhsa_exception_fp_ieee_invalid_op 0
		.amdhsa_exception_fp_denorm_src 0
		.amdhsa_exception_fp_ieee_div_zero 0
		.amdhsa_exception_fp_ieee_overflow 0
		.amdhsa_exception_fp_ieee_underflow 0
		.amdhsa_exception_fp_ieee_inexact 0
		.amdhsa_exception_int_div_zero 0
	.end_amdhsa_kernel

amdhsa.kernels:
  - .agpr_count:     0
    .args:
      - .actual_access:  read_only
        .address_space:  global
        .offset:         0
        .size:           8
        .value_kind:     global_buffer
      - .actual_access:  read_only
        .address_space:  global
        .offset:         8
        .size:           8
        .value_kind:     global_buffer
      - .actual_access:  read_only
        .address_space:  global
        .offset:         16
        .size:           8
        .value_kind:     global_buffer
      - .actual_access:  write_only
        .address_space:  global
        .offset:         24
        .size:           8
        .value_kind:     global_buffer
      - .actual_access:  write_only
        .address_space:  global
        .offset:         32
        .size:           8
        .value_kind:     global_buffer
      - .actual_access:  write_only
        .address_space:  global
        .offset:         40
        .size:           8
        .value_kind:     global_buffer
    .group_segment_fixed_size: 57344
    .kernarg_segment_align: 8
    .kernarg_segment_size: 48
    .language:       OpenCL C
    .language_version:
      - 2
      - 0
    .max_flat_workgroup_size: 512
    .name:           _Z12gemm1_kernelPKfS0_S0_PDv8_DF16_PDF16_S3_
    .private_segment_fixed_size: 0
    .sgpr_count:     18
    .sgpr_spill_count: 0
    .symbol:         _Z12gemm1_kernelPKfS0_S0_PDv8_DF16_PDF16_S3_.kd
    .uniform_work_group_size: 1
    .uses_dynamic_stack: false
    .vgpr_count:     125
    .vgpr_spill_count: 0
    .wavefront_size: 64
  - .agpr_count:     0
    .args:
      - .actual_access:  read_only
        .address_space:  global
        .offset:         0
        .size:           8
        .value_kind:     global_buffer
      - .actual_access:  read_only
        .address_space:  global
        .offset:         8
        .size:           8
        .value_kind:     global_buffer
      - .actual_access:  read_only
        .address_space:  global
        .offset:         16
        .size:           8
        .value_kind:     global_buffer
      - .actual_access:  read_only
        .address_space:  global
        .offset:         24
        .size:           8
        .value_kind:     global_buffer
      - .actual_access:  write_only
        .address_space:  global
        .offset:         32
        .size:           8
        .value_kind:     global_buffer
      - .actual_access:  write_only
        .address_space:  global
        .offset:         40
        .size:           8
        .value_kind:     global_buffer
    .group_segment_fixed_size: 87040
    .kernarg_segment_align: 8
    .kernarg_segment_size: 48
    .language:       OpenCL C
    .language_version:
      - 2
      - 0
    .max_flat_workgroup_size: 768
    .name:           _Z11attn_kernelPKiPKDv8_DF16_PKDF16_S5_PDF16_Pf
    .private_segment_fixed_size: 0
    .sgpr_count:     55
    .sgpr_spill_count: 0
    .symbol:         _Z11attn_kernelPKiPKDv8_DF16_PKDF16_S5_PDF16_Pf.kd
    .uniform_work_group_size: 1
    .uses_dynamic_stack: false
    .vgpr_count:     156
    .vgpr_spill_count: 0
    .wavefront_size: 64
  - .agpr_count:     12
    .args:
      - .actual_access:  read_only
        .address_space:  global
        .offset:         0
        .size:           8
        .value_kind:     global_buffer
      - .actual_access:  read_only
        .address_space:  global
        .offset:         8
        .size:           8
        .value_kind:     global_buffer
      - .actual_access:  read_only
        .address_space:  global
        .offset:         16
        .size:           8
        .value_kind:     global_buffer
      - .actual_access:  read_only
        .address_space:  global
        .offset:         24
        .size:           8
        .value_kind:     global_buffer
      - .actual_access:  read_only
        .address_space:  global
        .offset:         32
        .size:           8
        .value_kind:     global_buffer
      - .actual_access:  read_only
        .address_space:  global
        .offset:         40
        .size:           8
        .value_kind:     global_buffer
      - .actual_access:  write_only
        .address_space:  global
        .offset:         48
        .size:           8
        .value_kind:     global_buffer
    .group_segment_fixed_size: 16192
    .kernarg_segment_align: 8
    .kernarg_segment_size: 56
    .language:       OpenCL C
    .language_version:
      - 2
      - 0
    .max_flat_workgroup_size: 256
    .name:           _Z10epi_kernelPKDF16_PKfS2_S2_S2_S2_Pf
    .private_segment_fixed_size: 0
    .sgpr_count:     70
    .sgpr_spill_count: 0
    .symbol:         _Z10epi_kernelPKDF16_PKfS2_S2_S2_S2_Pf.kd
    .uniform_work_group_size: 1
    .uses_dynamic_stack: false
    .vgpr_count:     140
    .vgpr_spill_count: 0
    .wavefront_size: 64
